# indexer loop: packed v_pk_ashrrev_i16 (VOP3P between MFMAs) replaced by two SDWA v_ashrrev_i16 per dword, grouped to respect the dst_sel forwarding wait state
# baseline (speedup 1.0000x reference)
.LBB0_708:
	s_mov_b32 s0, 0x20000
	s_movk_i32 s1, 15
	s_add_i32 s52, s52, 16
	s_cmp_ge_i32 s52, s9
	v_add_u32_e32 v195, v201, v142
	v_add_u32_e32 v196, v202, v203
	s_waitcnt vmcnt(8)
	v_mfma_f32_16x16x32_bf16 v[114:117], v[134:137], v[66:69], 0
	v_mfma_f32_16x16x32_bf16 v[114:117], v[130:133], v[70:73], v[114:117]
	v_mfma_f32_16x16x32_bf16 v[74:77], v[134:137], v[2:5], 0
	v_mfma_f32_16x16x32_bf16 v[74:77], v[130:133], v[34:37], v[74:77]
	v_mfma_f32_16x16x32_bf16 v[78:81], v[134:137], v[6:9], 0
	v_mfma_f32_16x16x32_bf16 v[78:81], v[130:133], v[38:41], v[78:81]
	v_mfma_f32_16x16x32_bf16 v[82:85], v[134:137], v[10:13], 0
	v_mfma_f32_16x16x32_bf16 v[82:85], v[130:133], v[42:45], v[82:85]
	v_mfma_f32_16x16x32_bf16 v[86:89], v[134:137], v[14:17], 0
	v_mfma_f32_16x16x32_bf16 v[86:89], v[130:133], v[46:49], v[86:89]
	v_mfma_f32_16x16x32_bf16 v[98:101], v[134:137], v[18:21], 0
	v_mfma_f32_16x16x32_bf16 v[98:101], v[130:133], v[50:53], v[98:101]
	v_mfma_f32_16x16x32_bf16 v[102:105], v[134:137], v[22:25], 0
	v_mfma_f32_16x16x32_bf16 v[102:105], v[130:133], v[54:57], v[102:105]
	v_mfma_f32_16x16x32_bf16 v[224:227], v[134:137], v[26:29], 0
	v_fma_f32 v114, v156, |v74|, v114
	v_fma_f32 v115, v156, |v75|, v115
	v_fma_f32 v116, v156, |v76|, v116
	v_fma_f32 v117, v156, |v77|, v117
	v_fma_f32 v114, v158, |v78|, v114
	v_fma_f32 v115, v158, |v79|, v115
	v_fma_f32 v116, v158, |v80|, v116
	v_mfma_f32_16x16x32_bf16 v[224:227], v[130:133], v[58:61], v[224:227]
	v_fma_f32 v117, v158, |v81|, v117
	v_fma_f32 v114, v160, |v82|, v114
	v_fma_f32 v115, v160, |v83|, v115
	v_fma_f32 v116, v160, |v84|, v116
	v_fma_f32 v117, v160, |v85|, v117
	v_fma_f32 v114, v162, |v86|, v114
	v_fma_f32 v115, v162, |v87|, v115
	v_mfma_f32_16x16x32_bf16 v[228:231], v[134:137], v[30:33], 0
	v_fma_f32 v116, v162, |v88|, v116
	v_fma_f32 v117, v162, |v89|, v117
	v_fma_f32 v114, v164, |v98|, v114
	v_fma_f32 v115, v164, |v99|, v115
	v_fma_f32 v116, v164, |v100|, v116
	v_fma_f32 v117, v164, |v101|, v117
	v_fma_f32 v114, v166, |v102|, v114
	v_mfma_f32_16x16x32_bf16 v[228:231], v[130:133], v[62:65], v[228:231]
	v_fma_f32 v115, v166, |v103|, v115
	v_fma_f32 v116, v166, |v104|, v116
	v_fma_f32 v117, v166, |v105|, v117
	v_fma_f32 v114, v168, |v224|, v114
	v_fma_f32 v115, v168, |v225|, v115
	v_fma_f32 v116, v168, |v226|, v116
	v_fma_f32 v117, v168, |v227|, v117
	v_add_u32_e32 v194, -48, v157
	v_min_u32_e32 v194, 0x1fff, v194
	v_lshlrev_b32_e32 v140, 7, v194
	v_lshl_add_u64 v[192:193], v[172:173], 0, v[140:141]
	global_load_dwordx4 v[134:137], v[192:193], off
	global_load_dwordx4 v[130:133], v[192:193], off offset:1024
	s_waitcnt vmcnt(8)
	v_mfma_f32_16x16x32_bf16 v[118:121], v[126:129], v[66:69], 0
	v_fma_f32 v114, v170, |v228|, v114
	v_fma_f32 v115, v170, |v229|, v115
	v_fma_f32 v116, v170, |v230|, v116
	v_fma_f32 v117, v170, |v231|, v117
	v_cvt_pk_f16_f32 v184, v114, v115
	v_cvt_pk_f16_f32 v185, v116, v117
	v_mfma_f32_16x16x32_bf16 v[118:121], v[122:125], v[70:73], v[118:121]
	v_ashrrev_i16_sdwa v186, s1, v184 dst_sel:WORD_0 dst_unused:UNUSED_PAD src0_sel:DWORD src1_sel:WORD_0
	v_ashrrev_i16_sdwa v187, s1, v185 dst_sel:WORD_0 dst_unused:UNUSED_PAD src0_sel:DWORD src1_sel:WORD_0
	v_ashrrev_i16_sdwa v186, s1, v184 dst_sel:WORD_1 dst_unused:UNUSED_PRESERVE src0_sel:DWORD src1_sel:WORD_1
	v_ashrrev_i16_sdwa v187, s1, v185 dst_sel:WORD_1 dst_unused:UNUSED_PRESERVE src0_sel:DWORD src1_sel:WORD_1
	v_bitop3_b32 v176, v186, v184, s3 bitop3:0x36
	v_bitop3_b32 v177, v187, v185, s3 bitop3:0x36
	v_bfe_u32 v188, v176, 7, 9
	v_lshrrev_b32_e32 v189, 23, v176
	v_bfe_u32 v190, v177, 7, 9
	v_lshrrev_b32_e32 v191, 23, v177
	v_mfma_f32_16x16x32_bf16 v[74:77], v[126:129], v[2:5], 0
	v_lshl_add_u32 v188, v188, 2, v143
	v_lshl_add_u32 v189, v189, 2, v143
	v_lshl_add_u32 v190, v190, 2, v143
	v_lshl_add_u32 v191, v191, 2, v143
	ds_add_u32 v188, v206
	ds_add_u32 v189, v206
	ds_add_u32 v190, v206
	v_mfma_f32_16x16x32_bf16 v[74:77], v[122:125], v[34:37], v[74:77]
	ds_add_u32 v191, v206
	v_mfma_f32_16x16x32_bf16 v[78:81], v[126:129], v[6:9], 0
	v_mfma_f32_16x16x32_bf16 v[78:81], v[122:125], v[38:41], v[78:81]
	v_mfma_f32_16x16x32_bf16 v[82:85], v[126:129], v[10:13], 0
	v_mfma_f32_16x16x32_bf16 v[82:85], v[122:125], v[42:45], v[82:85]
	v_mfma_f32_16x16x32_bf16 v[86:89], v[126:129], v[14:17], 0
	v_mfma_f32_16x16x32_bf16 v[86:89], v[122:125], v[46:49], v[86:89]
	v_mfma_f32_16x16x32_bf16 v[98:101], v[126:129], v[18:21], 0
	v_mfma_f32_16x16x32_bf16 v[98:101], v[122:125], v[50:53], v[98:101]
	v_mfma_f32_16x16x32_bf16 v[102:105], v[126:129], v[22:25], 0
	v_mfma_f32_16x16x32_bf16 v[102:105], v[122:125], v[54:57], v[102:105]
	v_fma_f32 v118, v156, |v74|, v118
	v_fma_f32 v119, v156, |v75|, v119
	v_fma_f32 v120, v156, |v76|, v120
	v_fma_f32 v121, v156, |v77|, v121
	v_fma_f32 v118, v158, |v78|, v118
	v_fma_f32 v119, v158, |v79|, v119
	v_fma_f32 v120, v158, |v80|, v120
	v_mfma_f32_16x16x32_bf16 v[224:227], v[126:129], v[26:29], 0
	v_fma_f32 v121, v158, |v81|, v121
	v_fma_f32 v118, v160, |v82|, v118
	v_fma_f32 v119, v160, |v83|, v119
	v_fma_f32 v120, v160, |v84|, v120
	v_fma_f32 v121, v160, |v85|, v121
	v_fma_f32 v118, v162, |v86|, v118
	v_fma_f32 v119, v162, |v87|, v119
	v_mfma_f32_16x16x32_bf16 v[224:227], v[122:125], v[58:61], v[224:227]
	v_fma_f32 v120, v162, |v88|, v120
	v_fma_f32 v121, v162, |v89|, v121
	v_fma_f32 v118, v164, |v98|, v118
	v_fma_f32 v119, v164, |v99|, v119
	v_fma_f32 v120, v164, |v100|, v120
	v_fma_f32 v121, v164, |v101|, v121
	v_fma_f32 v118, v166, |v102|, v118
	v_mfma_f32_16x16x32_bf16 v[228:231], v[126:129], v[30:33], 0
	v_fma_f32 v119, v166, |v103|, v119
	v_fma_f32 v120, v166, |v104|, v120
	v_fma_f32 v121, v166, |v105|, v121
	v_fma_f32 v118, v168, |v224|, v118
	v_fma_f32 v119, v168, |v225|, v119
	v_fma_f32 v120, v168, |v226|, v120
	v_fma_f32 v121, v168, |v227|, v121
	v_mfma_f32_16x16x32_bf16 v[228:231], v[122:125], v[62:65], v[228:231]
	v_add_u32_e32 v194, -32, v157
	v_min_u32_e32 v194, 0x1fff, v194
	v_lshlrev_b32_e32 v140, 7, v194
	v_lshl_add_u64 v[192:193], v[172:173], 0, v[140:141]
	global_load_dwordx4 v[126:129], v[192:193], off
	global_load_dwordx4 v[122:125], v[192:193], off offset:1024
	s_waitcnt vmcnt(8)
	v_mfma_f32_16x16x32_bf16 v[114:117], v[110:113], v[66:69], 0
	v_mfma_f32_16x16x32_bf16 v[114:117], v[106:109], v[70:73], v[114:117]
	v_mfma_f32_16x16x32_bf16 v[74:77], v[110:113], v[2:5], 0
	v_mfma_f32_16x16x32_bf16 v[74:77], v[106:109], v[34:37], v[74:77]
	v_fma_f32 v118, v170, |v228|, v118
	v_fma_f32 v119, v170, |v229|, v119
	v_fma_f32 v120, v170, |v230|, v120
	v_fma_f32 v121, v170, |v231|, v121
	v_cvt_pk_f16_f32 v184, v118, v119
	v_cvt_pk_f16_f32 v185, v120, v121
	v_mfma_f32_16x16x32_bf16 v[78:81], v[110:113], v[6:9], 0
	v_ashrrev_i16_sdwa v186, s1, v184 dst_sel:WORD_0 dst_unused:UNUSED_PAD src0_sel:DWORD src1_sel:WORD_0
	v_ashrrev_i16_sdwa v187, s1, v185 dst_sel:WORD_0 dst_unused:UNUSED_PAD src0_sel:DWORD src1_sel:WORD_0
	v_ashrrev_i16_sdwa v186, s1, v184 dst_sel:WORD_1 dst_unused:UNUSED_PRESERVE src0_sel:DWORD src1_sel:WORD_1
	v_ashrrev_i16_sdwa v187, s1, v185 dst_sel:WORD_1 dst_unused:UNUSED_PRESERVE src0_sel:DWORD src1_sel:WORD_1
	v_bitop3_b32 v178, v186, v184, s3 bitop3:0x36
	v_bitop3_b32 v179, v187, v185, s3 bitop3:0x36
	v_bfe_u32 v188, v178, 7, 9
	v_lshrrev_b32_e32 v189, 23, v178
	v_bfe_u32 v190, v179, 7, 9
	v_lshrrev_b32_e32 v191, 23, v179
	v_mfma_f32_16x16x32_bf16 v[78:81], v[106:109], v[38:41], v[78:81]
	v_lshl_add_u32 v188, v188, 2, v143
	v_lshl_add_u32 v189, v189, 2, v143
	v_lshl_add_u32 v190, v190, 2, v143
	v_lshl_add_u32 v191, v191, 2, v143
	ds_add_u32 v188, v206
	ds_add_u32 v189, v206
	ds_add_u32 v190, v206
	v_mfma_f32_16x16x32_bf16 v[82:85], v[110:113], v[10:13], 0
	ds_add_u32 v191, v206
	v_fma_f32 v114, v156, |v74|, v114
	v_fma_f32 v115, v156, |v75|, v115
	v_fma_f32 v116, v156, |v76|, v116
	v_fma_f32 v117, v156, |v77|, v117
	v_fma_f32 v114, v158, |v78|, v114
	v_fma_f32 v115, v158, |v79|, v115
	v_mfma_f32_16x16x32_bf16 v[82:85], v[106:109], v[42:45], v[82:85]
	v_fma_f32 v116, v158, |v80|, v116
	v_fma_f32 v117, v158, |v81|, v117
	v_mfma_f32_16x16x32_bf16 v[86:89], v[110:113], v[14:17], 0
	v_mfma_f32_16x16x32_bf16 v[86:89], v[106:109], v[46:49], v[86:89]
	v_mfma_f32_16x16x32_bf16 v[98:101], v[110:113], v[18:21], 0
	v_mfma_f32_16x16x32_bf16 v[98:101], v[106:109], v[50:53], v[98:101]
	v_mfma_f32_16x16x32_bf16 v[102:105], v[110:113], v[22:25], 0
	v_mfma_f32_16x16x32_bf16 v[102:105], v[106:109], v[54:57], v[102:105]
	v_mfma_f32_16x16x32_bf16 v[224:227], v[110:113], v[26:29], 0
	v_mfma_f32_16x16x32_bf16 v[224:227], v[106:109], v[58:61], v[224:227]
	v_mfma_f32_16x16x32_bf16 v[228:231], v[110:113], v[30:33], 0
	v_fma_f32 v114, v160, |v82|, v114
	v_fma_f32 v115, v160, |v83|, v115
	v_fma_f32 v116, v160, |v84|, v116
	v_fma_f32 v117, v160, |v85|, v117
	v_fma_f32 v114, v162, |v86|, v114
	v_fma_f32 v115, v162, |v87|, v115
	v_fma_f32 v116, v162, |v88|, v116
	v_mfma_f32_16x16x32_bf16 v[228:231], v[106:109], v[62:65], v[228:231]
	v_fma_f32 v117, v162, |v89|, v117
	v_fma_f32 v114, v164, |v98|, v114
	v_fma_f32 v115, v164, |v99|, v115
	v_fma_f32 v116, v164, |v100|, v116
	v_fma_f32 v117, v164, |v101|, v117
	v_fma_f32 v114, v166, |v102|, v114
	v_fma_f32 v115, v166, |v103|, v115
	v_add_u32_e32 v194, -16, v157
	v_min_u32_e32 v194, 0x1fff, v194
	v_lshlrev_b32_e32 v140, 7, v194
	v_lshl_add_u64 v[192:193], v[172:173], 0, v[140:141]
	global_load_dwordx4 v[110:113], v[192:193], off
	global_load_dwordx4 v[106:109], v[192:193], off offset:1024
	s_waitcnt vmcnt(8)
	v_mfma_f32_16x16x32_bf16 v[118:121], v[94:97], v[66:69], 0
	v_fma_f32 v116, v166, |v104|, v116
	v_fma_f32 v117, v166, |v105|, v117
	v_fma_f32 v114, v168, |v224|, v114
	v_fma_f32 v115, v168, |v225|, v115
	v_fma_f32 v116, v168, |v226|, v116
	v_fma_f32 v117, v168, |v227|, v117
	v_fma_f32 v114, v170, |v228|, v114
	v_mfma_f32_16x16x32_bf16 v[118:121], v[90:93], v[70:73], v[118:121]
	v_fma_f32 v115, v170, |v229|, v115
	v_fma_f32 v116, v170, |v230|, v116
	v_fma_f32 v117, v170, |v231|, v117
	v_cvt_pk_f16_f32 v184, v114, v115
	v_cvt_pk_f16_f32 v185, v116, v117
	v_mfma_f32_16x16x32_bf16 v[74:77], v[94:97], v[2:5], 0
	v_ashrrev_i16_sdwa v186, s1, v184 dst_sel:WORD_0 dst_unused:UNUSED_PAD src0_sel:DWORD src1_sel:WORD_0
	v_ashrrev_i16_sdwa v187, s1, v185 dst_sel:WORD_0 dst_unused:UNUSED_PAD src0_sel:DWORD src1_sel:WORD_0
	v_ashrrev_i16_sdwa v186, s1, v184 dst_sel:WORD_1 dst_unused:UNUSED_PRESERVE src0_sel:DWORD src1_sel:WORD_1
	v_ashrrev_i16_sdwa v187, s1, v185 dst_sel:WORD_1 dst_unused:UNUSED_PRESERVE src0_sel:DWORD src1_sel:WORD_1
	v_bitop3_b32 v180, v186, v184, s3 bitop3:0x36
	v_bitop3_b32 v181, v187, v185, s3 bitop3:0x36
	v_bfe_u32 v188, v180, 7, 9
	v_lshrrev_b32_e32 v189, 23, v180
	v_bfe_u32 v190, v181, 7, 9
	v_lshrrev_b32_e32 v191, 23, v181
	v_lshl_add_u32 v188, v188, 2, v143
	v_mfma_f32_16x16x32_bf16 v[74:77], v[90:93], v[34:37], v[74:77]
	v_lshl_add_u32 v189, v189, 2, v143
	v_lshl_add_u32 v190, v190, 2, v143
	v_lshl_add_u32 v191, v191, 2, v143
	ds_add_u32 v188, v206
	ds_add_u32 v189, v206
	ds_add_u32 v190, v206
	ds_add_u32 v191, v206
	v_mfma_f32_16x16x32_bf16 v[78:81], v[94:97], v[6:9], 0
	v_mfma_f32_16x16x32_bf16 v[78:81], v[90:93], v[38:41], v[78:81]
	v_mfma_f32_16x16x32_bf16 v[82:85], v[94:97], v[10:13], 0
	v_mfma_f32_16x16x32_bf16 v[82:85], v[90:93], v[42:45], v[82:85]
	v_fma_f32 v118, v156, |v74|, v118
	v_fma_f32 v119, v156, |v75|, v119
	v_fma_f32 v120, v156, |v76|, v120
	v_fma_f32 v121, v156, |v77|, v121
	v_mfma_f32_16x16x32_bf16 v[86:89], v[94:97], v[14:17], 0
	v_mfma_f32_16x16x32_bf16 v[86:89], v[90:93], v[46:49], v[86:89]
	v_mfma_f32_16x16x32_bf16 v[98:101], v[94:97], v[18:21], 0
	v_mfma_f32_16x16x32_bf16 v[98:101], v[90:93], v[50:53], v[98:101]
	v_mfma_f32_16x16x32_bf16 v[102:105], v[94:97], v[22:25], 0
	v_fma_f32 v118, v158, |v78|, v118
	v_fma_f32 v119, v158, |v79|, v119
	v_fma_f32 v120, v158, |v80|, v120
	v_fma_f32 v121, v158, |v81|, v121
	v_fma_f32 v118, v160, |v82|, v118
	v_fma_f32 v119, v160, |v83|, v119
	v_fma_f32 v120, v160, |v84|, v120
	v_mfma_f32_16x16x32_bf16 v[102:105], v[90:93], v[54:57], v[102:105]
	v_fma_f32 v121, v160, |v85|, v121
	v_fma_f32 v118, v162, |v86|, v118
	v_fma_f32 v119, v162, |v87|, v119
	v_fma_f32 v120, v162, |v88|, v120
	v_fma_f32 v121, v162, |v89|, v121
	v_fma_f32 v118, v164, |v98|, v118
	v_fma_f32 v119, v164, |v99|, v119
	v_mfma_f32_16x16x32_bf16 v[224:227], v[94:97], v[26:29], 0
	v_fma_f32 v120, v164, |v100|, v120
	v_fma_f32 v121, v164, |v101|, v121
	v_mfma_f32_16x16x32_bf16 v[224:227], v[90:93], v[58:61], v[224:227]
	v_fma_f32 v118, v166, |v102|, v118
	v_fma_f32 v119, v166, |v103|, v119
	v_fma_f32 v120, v166, |v104|, v120
	v_fma_f32 v121, v166, |v105|, v121
	v_mfma_f32_16x16x32_bf16 v[228:231], v[94:97], v[30:33], 0
	v_mfma_f32_16x16x32_bf16 v[228:231], v[90:93], v[62:65], v[228:231]
	s_nop 4
	v_fma_f32 v118, v168, |v224|, v118
	v_fma_f32 v119, v168, |v225|, v119
	v_fma_f32 v120, v168, |v226|, v120
	v_fma_f32 v121, v168, |v227|, v121
	s_nop 1
	v_fma_f32 v118, v170, |v228|, v118
	v_fma_f32 v119, v170, |v229|, v119
	v_fma_f32 v120, v170, |v230|, v120
	v_fma_f32 v121, v170, |v231|, v121
	v_cvt_pk_f16_f32 v184, v118, v119
	v_cvt_pk_f16_f32 v185, v120, v121
	v_ashrrev_i16_sdwa v186, s1, v184 dst_sel:WORD_0 dst_unused:UNUSED_PAD src0_sel:DWORD src1_sel:WORD_0
	v_ashrrev_i16_sdwa v187, s1, v185 dst_sel:WORD_0 dst_unused:UNUSED_PAD src0_sel:DWORD src1_sel:WORD_0
	v_ashrrev_i16_sdwa v186, s1, v184 dst_sel:WORD_1 dst_unused:UNUSED_PRESERVE src0_sel:DWORD src1_sel:WORD_1
	v_ashrrev_i16_sdwa v187, s1, v185 dst_sel:WORD_1 dst_unused:UNUSED_PRESERVE src0_sel:DWORD src1_sel:WORD_1
	v_bitop3_b32 v182, v186, v184, s3 bitop3:0x36
	v_bitop3_b32 v183, v187, v185, s3 bitop3:0x36
	v_bfe_u32 v188, v182, 7, 9
	v_lshrrev_b32_e32 v189, 23, v182
	v_bfe_u32 v190, v183, 7, 9
	v_lshrrev_b32_e32 v191, 23, v183
	v_lshl_add_u32 v188, v188, 2, v143
	v_lshl_add_u32 v189, v189, 2, v143
	v_lshl_add_u32 v190, v190, 2, v143
	v_lshl_add_u32 v191, v191, 2, v143
	ds_add_u32 v188, v206
	ds_add_u32 v189, v206
	ds_add_u32 v190, v206
	ds_add_u32 v191, v206
	v_mov_b32_e32 v194, v157
	v_min_u32_e32 v194, 0x1fff, v194
	v_lshlrev_b32_e32 v140, 7, v194
	v_lshl_add_u64 v[192:193], v[172:173], 0, v[140:141]
	global_load_dwordx4 v[94:97], v[192:193], off
	global_load_dwordx4 v[90:93], v[192:193], off offset:1024
	v_add_u32_e32 v157, 0x100, v157
	ds_write2_b64 v195, v[176:177], v[178:179] offset1:4
	ds_write2_b64 v195, v[180:181], v[182:183] offset0:8 offset1:12
	s_waitcnt lgkmcnt(0)
	ds_read_b128 v[232:235], v196
	ds_read_b128 v[236:239], v196 offset:1152
	s_waitcnt lgkmcnt(1)
	global_store_dwordx4 v[174:175], v[232:235], off
	v_add_co_u32_e32 v198, vcc, s0, v174
	s_nop 1
	v_addc_co_u32_e32 v199, vcc, 0, v175, vcc
	s_waitcnt lgkmcnt(0)
	global_store_dwordx4 v[198:199], v[236:239], off
	v_lshl_add_u64 v[174:175], v[174:175], 0, s[14:15]
	s_cbranch_scc0 .LBB0_708
	s_waitcnt vmcnt(2)
	v_mov_b64_e32 v[118:119], v[134:135]
	v_mov_b64_e32 v[120:121], v[136:137]
	v_mov_b64_e32 v[114:115], v[130:131]
	v_mov_b64_e32 v[116:117], v[132:133]
	v_mov_b64_e32 v[102:103], v[126:127]
	v_mov_b64_e32 v[104:105], v[128:129]
	v_mov_b64_e32 v[98:99], v[122:123]
	v_mov_b64_e32 v[100:101], v[124:125]
	v_mov_b64_e32 v[86:87], v[110:111]
	v_mov_b64_e32 v[88:89], v[112:113]
	v_mov_b64_e32 v[82:83], v[106:107]
	v_mov_b64_e32 v[84:85], v[108:109]
	v_mov_b64_e32 v[78:79], v[94:95]
	v_mov_b64_e32 v[80:81], v[96:97]
	v_mov_b64_e32 v[74:75], v[90:91]
	v_mov_b64_e32 v[76:77], v[92:93]
	s_branch .LBB0_710
